# attention<0> tile loop unrolled by LDS buffer parity: K/V read addresses become loop-invariant registers plus immediate offsets, 14 address adds per tile removed
# speedup vs baseline: 1.0088x; 1.0088x over previous
.LBB0_1247:
	v_readlane_b32 s0, v251, 54
	v_readlane_b32 s1, v251, 55
	s_andn2_b64 vcc, exec, s[0:1]
	v_readfirstlane_b32 s0, v219
	s_waitcnt lgkmcnt(0)
	s_barrier
	s_cbranch_vccnz .LBB0_1263
	v_bfe_u32 v3, v219, 4, 2
	v_lshrrev_b32_e32 v2, 4, v219
	v_lshlrev_b32_e32 v0, 3, v3
	v_mov_b32_e32 v1, v33
	v_lshlrev_b32_e32 v170, 2, v3
	v_lshl_add_u64 v[172:173], s[4:5], 0, v[0:1]
	v_bitop3_b32 v1, v2, v166, 3 bitop3:0x6c
	s_waitcnt vmcnt(14)
	v_lshrrev_b32_e32 v4, 2, v219
	v_or_b32_e32 v5, v170, v163
	v_lshlrev_b32_e32 v222, 4, v1
	v_bitop3_b32 v1, v3, v166, 4 bitop3:0x36
	v_and_or_b32 v4, v4, 4, v163
	v_lshlrev_b32_e32 v5, 8, v5
	v_and_b32_e32 v6, 8, v220
	v_lshlrev_b32_e32 v223, 4, v1
	v_bitop3_b32 v1, v3, v166, 8 bitop3:0x36
	v_lshlrev_b32_e32 v4, 1, v4
	v_add3_u32 v221, 0, v5, v6
	v_bfe_u32 v5, v219, 1, 1
	v_lshlrev_b32_e32 v224, 4, v1
	v_bitop3_b32 v1, v3, v166, 12 bitop3:0x36
	v_lshlrev_b32_e32 v225, 4, v1
	v_or_b32_e32 v1, v4, v5
	v_lshlrev_b32_e32 v237, 4, v1
	v_bitop3_b32 v1, v4, v5, 2 bitop3:0x1e
	v_lshlrev_b32_e32 v238, 4, v1
	v_bitop3_b32 v1, v4, v5, 4 bitop3:0x1e
	v_lshlrev_b32_e32 v239, 4, v1
	v_bitop3_b32 v1, v4, v5, 6 bitop3:0x1e
	v_lshlrev_b32_e32 v240, 4, v1
	v_bitop3_b32 v1, v4, v5, 8 bitop3:0x1e
	v_lshlrev_b32_e32 v241, 4, v1
	v_bitop3_b32 v1, v4, v5, 10 bitop3:0x1e
	v_lshlrev_b32_e32 v242, 4, v1
	v_bitop3_b32 v1, v4, v5, 12 bitop3:0x1e
	s_ashr_i32 s14, s0, 6
	v_lshlrev_b32_e32 v243, 4, v1
	v_bitop3_b32 v1, v4, v5, 14 bitop3:0x1e
	s_lshl_b32 s15, s14, 3
	v_lshlrev_b32_e32 v244, 4, v1
	v_or_b32_e32 v1, s15, v3
	v_lshlrev_b32_e32 v4, 3, v166
	v_lshlrev_b32_e32 v5, 4, v3
	s_and_b32 s20, s0, 0xffffff80
	s_lshl_b32 s0, s14, 5
	v_xor_b32_e32 v4, v5, v4
	v_or_b32_e32 v5, 4, v1
	v_and_or_b32 v245, s0, 32, v166
	v_mad_i64_i32 v[180:181], s[0:1], v1, s96, 0
	v_mad_i64_i32 v[182:183], s[0:1], v5, s96, 0
	v_bitop3_b32 v1, v1, v219, 4 bitop3:0x36
	v_lshlrev_b32_e32 v1, 3, v1
	s_lshl_b32 s0, s14, 14
	v_bitop3_b32 v2, s15, v219, v3 bitop3:0x36
	v_and_b32_e32 v6, 0x78, v1
	v_lshlrev_b32_e32 v1, 1, v5
	s_and_b32 s0, s0, 0x4000
	s_lshl_b32 s16, s14, 11
	v_lshlrev_b32_e32 v2, 3, v2
	v_bitop3_b32 v1, v1, v166, 14 bitop3:0x6c
	s_add_i32 s0, s0, 0
	v_add_u32_e32 v174, 0x2000, v168
	v_add_u32_e32 v176, 0x4000, v168
	v_add_u32_e32 v178, 0x6000, v168
	v_and_b32_e32 v2, 0x78, v2
	s_add_i32 s21, s16, 0
	s_waitcnt vmcnt(13)
	v_lshlrev_b32_e32 v8, 3, v1
	s_add_i32 s0, s0, 0x10000
	s_addk_i32 s15, 0x44
	v_lshl_add_u32 v171, v166, 8, 0
	v_ashrrev_i32_e32 v169, 31, v168
	v_ashrrev_i32_e32 v175, 31, v174
	v_ashrrev_i32_e32 v177, 31, v176
	v_ashrrev_i32_e32 v179, 31, v178
	v_lshl_add_u32 v246, v166, 9, s0
	v_or_b32_e32 v247, s15, v3
	v_lshlrev_b32_e32 v32, 1, v2
	v_lshlrev_b32_e32 v184, 1, v4
	v_lshlrev_b32_e32 v186, 1, v6
	v_lshlrev_b32_e32 v188, 1, v8
	v_add3_u32 v32, v180, v32, s84
	v_add3_u32 v184, v180, v184, s90
	v_add3_u32 v186, v182, v186, s84
	v_add3_u32 v188, v182, v188, s90
	v_lshlrev_b32_e32 v190, 1, v0
	v_add_u32_e32 v222, v171, v222
	v_add_u32_e32 v223, v171, v223
	v_add_u32_e32 v224, v171, v224
	v_add_u32_e32 v225, v171, v225
	v_add_u32_e32 v237, v221, v237
	v_add_u32_e32 v238, v221, v238
	v_add_u32_e32 v239, v221, v239
	v_add_u32_e32 v240, v221, v240
	v_add_u32_e32 v241, v221, v241
	v_add_u32_e32 v242, v221, v242
	v_add_u32_e32 v243, v221, v243
	v_add_u32_e32 v244, v221, v244
	s_add_i32 s22, s21, 0x8400
	s_mov_b32 s23, s83
	s_branch .LBB0_1250

.LBB0_1255:
	s_mov_b64 s[18:19], 0
.LBB0_1256:
	s_andn2_b64 vcc, exec, s[18:19]
	s_cbranch_vccnz .LBB0_1258
	s_add_i32 s34, s21, 0x4000
	s_mov_b32 m0, s34
	s_nop 0
	global_load_lds_dwordx4 v32, s[100:101]
	s_add_i32 m0, s34, 0x8000
	s_nop 0
	global_load_lds_dwordx4 v184, s[100:101]
	s_add_i32 m0, s34, 0x400
	s_nop 0
	global_load_lds_dwordx4 v186, s[100:101]
	s_add_i32 m0, s34, 0x8400
	s_nop 0
	global_load_lds_dwordx4 v188, s[100:101]
	s_add_u32 s100, s100, 0x240000
	s_addc_u32 s101, s101, 0
.LBB0_1258:
	ds_read_b128 v[102:105], v222
	ds_read_b128 v[106:109], v223
	ds_read_b128 v[110:113], v224
	ds_read_b128 v[114:117], v225
	ds_read_b128 v[118:121], v222 offset:4096
	ds_read_b128 v[122:125], v223 offset:4096
	ds_read_b128 v[126:129], v224 offset:4096
	ds_read_b128 v[130:133], v225 offset:4096
	s_waitcnt lgkmcnt(0)
	v_mfma_f32_16x16x32_bf16 v[138:141], v[118:121], v[78:81], 0
	v_mfma_f32_16x16x32_bf16 v[134:137], v[102:105], v[78:81], 0
	v_mfma_f32_16x16x32_bf16 v[102:105], v[102:105], v[94:97], 0
	v_mfma_f32_16x16x32_bf16 v[118:121], v[118:121], v[94:97], 0
	v_mfma_f32_16x16x32_bf16 v[134:137], v[106:109], v[70:73], v[134:137]
	v_mfma_f32_16x16x32_bf16 v[102:105], v[106:109], v[86:89], v[102:105]
	v_mfma_f32_16x16x32_bf16 v[138:141], v[122:125], v[70:73], v[138:141]
	v_mfma_f32_16x16x32_bf16 v[118:121], v[122:125], v[86:89], v[118:121]
	v_mfma_f32_16x16x32_bf16 v[134:137], v[110:113], v[74:77], v[134:137]
	v_mfma_f32_16x16x32_bf16 v[102:105], v[110:113], v[90:93], v[102:105]
	v_mfma_f32_16x16x32_bf16 v[138:141], v[126:129], v[74:77], v[138:141]
	v_mfma_f32_16x16x32_bf16 v[118:121], v[126:129], v[90:93], v[118:121]
	v_mfma_f32_16x16x32_bf16 v[162:165], v[114:117], v[82:85], v[134:137]
	v_mfma_f32_16x16x32_bf16 v[134:137], v[114:117], v[98:101], v[102:105]
	s_nop 3
	ds_read_b128 v[102:105], v222 offset:8192
	ds_read_b128 v[106:109], v223 offset:8192
	ds_read_b128 v[110:113], v224 offset:8192
	ds_read_b128 v[114:117], v225 offset:8192
	v_max_f32_e32 v187, v164, v165
	v_mfma_f32_16x16x32_bf16 v[158:161], v[130:133], v[82:85], v[138:141]
	v_max3_f32 v187, v162, v163, v187
	v_mfma_f32_16x16x32_bf16 v[138:141], v[130:133], v[98:101], v[118:121]
	s_nop 2
	ds_read_b128 v[118:121], v222 offset:12288
	ds_read_b128 v[122:125], v223 offset:12288
	ds_read_b128 v[126:129], v224 offset:12288
	ds_read_b128 v[130:133], v225 offset:12288
	v_max3_f32 v189, v159, v160, v161
	v_max3_f32 v187, v187, v158, v189
	s_waitcnt lgkmcnt(0)
	v_mfma_f32_16x16x32_bf16 v[142:145], v[102:105], v[78:81], 0
	v_mfma_f32_16x16x32_bf16 v[102:105], v[102:105], v[94:97], 0
	v_mfma_f32_16x16x32_bf16 v[102:105], v[106:109], v[86:89], v[102:105]
	v_mfma_f32_16x16x32_bf16 v[102:105], v[110:113], v[90:93], v[102:105]
	v_mfma_f32_16x16x32_bf16 v[146:149], v[114:117], v[98:101], v[102:105]
	v_mfma_f32_16x16x32_bf16 v[102:105], v[118:121], v[78:81], 0
	v_mfma_f32_16x16x32_bf16 v[142:145], v[106:109], v[70:73], v[142:145]
	v_mfma_f32_16x16x32_bf16 v[102:105], v[122:125], v[70:73], v[102:105]
	v_mfma_f32_16x16x32_bf16 v[142:145], v[110:113], v[74:77], v[142:145]
	v_mfma_f32_16x16x32_bf16 v[102:105], v[126:129], v[74:77], v[102:105]
	v_mfma_f32_16x16x32_bf16 v[154:157], v[114:117], v[82:85], v[142:145]
	v_mfma_f32_16x16x32_bf16 v[150:153], v[130:133], v[82:85], v[102:105]
	v_mfma_f32_16x16x32_bf16 v[102:105], v[118:121], v[94:97], 0
	s_nop 5
	v_max3_f32 v189, v155, v156, v157
	v_max3_f32 v187, v187, v154, v189
	v_max3_f32 v189, v151, v152, v153
	v_mfma_f32_16x16x32_bf16 v[102:105], v[122:125], v[86:89], v[102:105]
	v_max3_f32 v187, v187, v150, v189
	v_mov_b32_e32 v189, v187
	s_nop 1
	v_permlane16_swap_b32_e32 v187, v189
	v_mfma_f32_16x16x32_bf16 v[102:105], v[126:129], v[90:93], v[102:105]
	v_max_f32 v187, v187, v189
	s_nop 0
	v_mov_b32_e32 v189, v187
	s_nop 1
	v_permlane32_swap_b32_e32 v187, v189
	v_max_f32 v187, v187, v189
	v_mfma_f32_16x16x32_bf16 v[142:145], v[130:133], v[98:101], v[102:105]
	v_mul_f32_e32 v187, 0x3e0293ee, v187
	v_add_f32_e32 v189, 0x41000000, v218
	v_cmp_gt_f32_e32 vcc, v187, v189
	ds_read_b64_tr_b16 v[130:131], v237 offset:32768
	ds_read_b64_tr_b16 v[132:133], v237 offset:36864
	ds_read_b64_tr_b16 v[122:123], v237 offset:40960
	ds_read_b64_tr_b16 v[124:125], v237 offset:45056
	ds_read_b64_tr_b16 v[126:127], v238 offset:32768
	ds_read_b64_tr_b16 v[128:129], v238 offset:36864
	ds_read_b64_tr_b16 v[114:115], v238 offset:40960
	ds_read_b64_tr_b16 v[116:117], v238 offset:45056
	v_cndmask_b32_e32 v187, v218, v187, vcc
	ds_read_b64_tr_b16 v[118:119], v239 offset:32768
	ds_read_b64_tr_b16 v[120:121], v239 offset:36864
	ds_read_b64_tr_b16 v[110:111], v239 offset:40960
	ds_read_b64_tr_b16 v[112:113], v239 offset:45056
	ds_read_b64_tr_b16 v[106:107], v240 offset:32768
	ds_read_b64_tr_b16 v[108:109], v240 offset:36864
	ds_read_b64_tr_b16 v[102:103], v240 offset:40960
	ds_read_b64_tr_b16 v[104:105], v240 offset:45056
	ds_read_b64 v[198:199], v213
	v_fma_f32 v162, v162, s97, -v187
	v_exp_f32_e32 v162, v162
	v_fma_f32 v163, v163, s97, -v187
	v_exp_f32_e32 v163, v163
	v_fma_f32 v164, v164, s97, -v187
	v_exp_f32_e32 v164, v164
	v_fma_f32 v165, v165, s97, -v187
	v_exp_f32_e32 v165, v165
	v_fma_f32 v158, v158, s97, -v187
	s_waitcnt lgkmcnt(0)
	v_lshrrev_b64 v[216:217], v170, v[198:199]
	v_bfe_i32 v198, v216, 0, 1
	v_exp_f32_e32 v158, v158
	v_and_b32_e32 v162, v198, v162
	v_fma_f32 v159, v159, s97, -v187
	v_bfe_i32 v199, v216, 1, 1
	v_and_b32_e32 v163, v199, v163
	v_exp_f32_e32 v159, v159
	v_fma_f32 v160, v160, s97, -v187
	v_add_f32_e32 v198, v162, v163
	v_bfe_i32 v199, v216, 2, 1
	v_exp_f32_e32 v160, v160
	v_and_b32_e32 v164, v199, v164
	v_fma_f32 v161, v161, s97, -v187
	v_bfe_i32 v200, v216, 3, 1
	v_add_f32_e32 v198, v198, v164
	v_and_b32_e32 v165, v200, v165
	v_exp_f32_e32 v161, v161
	v_fma_f32 v154, v154, s97, -v187
	v_add_f32_e32 v198, v198, v165
	v_bfe_i32 v199, v216, 16, 1
	v_exp_f32_e32 v154, v154
	v_and_b32_e32 v158, v199, v158
	v_fma_f32 v155, v155, s97, -v187
	v_bfe_i32 v200, v216, 17, 1
	v_add_f32_e32 v198, v198, v158
	v_and_b32_e32 v159, v200, v159
	v_exp_f32_e32 v155, v155
	v_fma_f32 v156, v156, s97, -v187
	v_add_f32_e32 v198, v198, v159
	v_bfe_i32 v199, v216, 18, 1
	v_exp_f32_e32 v156, v156
	v_and_b32_e32 v160, v199, v160
	v_fma_f32 v157, v157, s97, -v187
	v_bfe_i32 v200, v216, 19, 1
	v_add_f32_e32 v198, v198, v160
	v_and_b32_e32 v161, v200, v161
	v_exp_f32_e32 v157, v157
	v_add_f32_e32 v198, v198, v161
	v_bfe_i32 v199, v217, 0, 1
	v_fma_f32 v150, v150, s97, -v187
	v_and_b32_e32 v154, v199, v154
	v_bfe_i32 v200, v217, 1, 1
	v_add_f32_e32 v198, v198, v154
	v_and_b32_e32 v155, v200, v155
	v_exp_f32_e32 v150, v150
	v_fma_f32 v151, v151, s97, -v187
	v_add_f32_e32 v198, v198, v155
	v_bfe_i32 v199, v217, 2, 1
	v_exp_f32_e32 v151, v151
	v_and_b32_e32 v216, v199, v156
	v_fma_f32 v152, v152, s97, -v187
	v_bfe_i32 v200, v217, 3, 1
	v_add_f32_e32 v156, v198, v216
	v_and_b32_e32 v157, v200, v157
	v_exp_f32_e32 v152, v152
	v_fma_f32 v153, v153, s97, -v187
	v_add_f32_e32 v198, v156, v157
	v_bfe_i32 v156, v217, 16, 1
	v_exp_f32_e32 v153, v153
	v_and_b32_e32 v156, v156, v150
	v_bfe_i32 v199, v217, 17, 1
	v_add_f32_e32 v150, v198, v156
	v_and_b32_e32 v151, v199, v151
	v_add_f32_e32 v150, v150, v151
	v_bfe_i32 v198, v217, 18, 1
	v_sub_f32_e32 v189, v218, v187
	v_and_b32_e32 v152, v198, v152
	v_bfe_i32 v199, v217, 19, 1
	v_add_f32_e32 v150, v150, v152
	v_and_b32_e32 v153, v199, v153
	v_add_f32_e32 v198, v150, v153
	v_exp_f32_e32 v150, v189
	s_nop 0
	v_cmp_eq_f32_e32 vcc, 1.0, v150
	v_fma_f32 v215, v215, v150, v198
	s_cmp_eq_u64 vcc, exec
	s_cbranch_scc1 .LBB0_1260
	v_pk_mul_f32 v[68:69], v[68:69], v[150:151] op_sel_hi:[1,0]
	v_pk_mul_f32 v[66:67], v[66:67], v[150:151] op_sel_hi:[1,0]
	v_pk_mul_f32 v[64:65], v[64:65], v[150:151] op_sel_hi:[1,0]
	v_pk_mul_f32 v[62:63], v[62:63], v[150:151] op_sel_hi:[1,0]
	v_pk_mul_f32 v[60:61], v[60:61], v[150:151] op_sel_hi:[1,0]
	v_pk_mul_f32 v[58:59], v[58:59], v[150:151] op_sel_hi:[1,0]
	v_pk_mul_f32 v[56:57], v[56:57], v[150:151] op_sel_hi:[1,0]
	v_pk_mul_f32 v[54:55], v[54:55], v[150:151] op_sel_hi:[1,0]
	v_pk_mul_f32 v[52:53], v[52:53], v[150:151] op_sel_hi:[1,0]
	v_pk_mul_f32 v[50:51], v[50:51], v[150:151] op_sel_hi:[1,0]
	v_pk_mul_f32 v[48:49], v[48:49], v[150:151] op_sel_hi:[1,0]
	v_pk_mul_f32 v[46:47], v[46:47], v[150:151] op_sel_hi:[1,0]
	v_pk_mul_f32 v[44:45], v[44:45], v[150:151] op_sel_hi:[1,0]
	v_pk_mul_f32 v[42:43], v[42:43], v[150:151] op_sel_hi:[1,0]
	v_pk_mul_f32 v[40:41], v[40:41], v[150:151] op_sel_hi:[1,0]
	v_pk_mul_f32 v[38:39], v[38:39], v[150:151] op_sel_hi:[1,0]

.LBB0_1262:
	v_cvt_pk_bf16_f32 v162, v162, v163
	v_cvt_pk_bf16_f32 v163, v164, v165
	v_cvt_pk_bf16_f32 v164, v158, v159
	v_cvt_pk_bf16_f32 v165, v160, v161
	v_cvt_pk_bf16_f32 v158, v218, v167
	v_cvt_pk_bf16_f32 v159, v136, v135
	v_cvt_pk_bf16_f32 v160, v138, v137
	v_cvt_pk_bf16_f32 v161, v140, v139
	v_mfma_f32_16x16x32_bf16 v[54:57], v[106:109], v[162:165], v[54:57]
	v_cvt_pk_bf16_f32 v154, v154, v155
	v_cvt_pk_bf16_f32 v155, v216, v157
	v_cvt_pk_bf16_f32 v156, v156, v151
	v_mfma_f32_16x16x32_bf16 v[16:19], v[106:109], v[158:161], v[16:19]
	v_cvt_pk_bf16_f32 v157, v152, v153
	s_add_i32 s31, s31, 1
	v_mfma_f32_16x16x32_bf16 v[66:69], v[130:133], v[162:165], v[66:69]
	v_add_u32_e32 v213, 8, v213
	s_cmp_eq_u32 s30, s31
	v_mfma_f32_16x16x32_bf16 v[28:31], v[130:133], v[158:161], v[28:31]
	v_cvt_pk_bf16_f32 v130, v146, v141
	v_cvt_pk_bf16_f32 v131, v148, v147
	v_cvt_pk_bf16_f32 v132, v142, v143
	v_cvt_pk_bf16_f32 v133, v144, v145
	v_mfma_f32_16x16x32_bf16 v[54:57], v[102:105], v[154:157], v[54:57]
	s_nop 0
	v_mfma_f32_16x16x32_bf16 v[16:19], v[102:105], v[130:133], v[16:19]
	ds_read_b64_tr_b16 v[102:103], v241 offset:32768
	ds_read_b64_tr_b16 v[104:105], v241 offset:36864
	ds_read_b64_tr_b16 v[106:107], v241 offset:40960
	ds_read_b64_tr_b16 v[108:109], v241 offset:45056
	v_mfma_f32_16x16x32_bf16 v[58:61], v[118:121], v[162:165], v[58:61]
	v_mfma_f32_16x16x32_bf16 v[20:23], v[118:121], v[158:161], v[20:23]
	s_waitcnt lgkmcnt(2)
	v_mfma_f32_16x16x32_bf16 v[50:53], v[102:105], v[162:165], v[50:53]
	v_mfma_f32_16x16x32_bf16 v[12:15], v[102:105], v[158:161], v[12:15]
	v_mfma_f32_16x16x32_bf16 v[58:61], v[110:113], v[154:157], v[58:61]
	v_mfma_f32_16x16x32_bf16 v[20:23], v[110:113], v[130:133], v[20:23]
	s_waitcnt lgkmcnt(0)
	v_mfma_f32_16x16x32_bf16 v[50:53], v[106:109], v[154:157], v[50:53]
	v_mfma_f32_16x16x32_bf16 v[12:15], v[106:109], v[130:133], v[12:15]
	ds_read_b64_tr_b16 v[102:103], v242 offset:32768
	ds_read_b64_tr_b16 v[104:105], v242 offset:36864
	ds_read_b64_tr_b16 v[106:107], v242 offset:40960
	ds_read_b64_tr_b16 v[108:109], v242 offset:45056
	s_waitcnt lgkmcnt(2)
	v_mfma_f32_16x16x32_bf16 v[46:49], v[102:105], v[162:165], v[46:49]
	v_mfma_f32_16x16x32_bf16 v[8:11], v[102:105], v[158:161], v[8:11]
	s_waitcnt lgkmcnt(0)
	v_mfma_f32_16x16x32_bf16 v[46:49], v[106:109], v[154:157], v[46:49]
	v_mfma_f32_16x16x32_bf16 v[8:11], v[106:109], v[130:133], v[8:11]
	ds_read_b64_tr_b16 v[102:103], v243 offset:32768
	ds_read_b64_tr_b16 v[104:105], v243 offset:36864
	ds_read_b64_tr_b16 v[106:107], v243 offset:40960
	ds_read_b64_tr_b16 v[108:109], v243 offset:45056
	s_waitcnt lgkmcnt(2)
	v_mfma_f32_16x16x32_bf16 v[42:45], v[102:105], v[162:165], v[42:45]
	v_mfma_f32_16x16x32_bf16 v[4:7], v[102:105], v[158:161], v[4:7]
	ds_read_b64_tr_b16 v[110:111], v244 offset:32768
	ds_read_b64_tr_b16 v[112:113], v244 offset:36864
	s_waitcnt lgkmcnt(2)
	v_mfma_f32_16x16x32_bf16 v[42:45], v[106:109], v[154:157], v[42:45]
	v_mfma_f32_16x16x32_bf16 v[4:7], v[106:109], v[130:133], v[4:7]
	ds_read_b64_tr_b16 v[104:105], v244 offset:40960
	ds_read_b64_tr_b16 v[106:107], v244 offset:45056
	s_waitcnt vmcnt(0)
	v_mfma_f32_16x16x32_bf16 v[62:65], v[126:129], v[162:165], v[62:65]
	s_waitcnt lgkmcnt(0)
	s_barrier
	v_mfma_f32_16x16x32_bf16 v[24:27], v[126:129], v[158:161], v[24:27]
	v_mfma_f32_16x16x32_bf16 v[38:41], v[110:113], v[162:165], v[38:41]
	v_mfma_f32_16x16x32_bf16 v[0:3], v[110:113], v[158:161], v[0:3]
	v_mfma_f32_16x16x32_bf16 v[66:69], v[122:125], v[154:157], v[66:69]
	v_mfma_f32_16x16x32_bf16 v[28:31], v[122:125], v[130:133], v[28:31]
	v_mfma_f32_16x16x32_bf16 v[62:65], v[114:117], v[154:157], v[62:65]
	v_mfma_f32_16x16x32_bf16 v[24:27], v[114:117], v[130:133], v[24:27]
	v_mfma_f32_16x16x32_bf16 v[38:41], v[104:107], v[154:157], v[38:41]
	v_mfma_f32_16x16x32_bf16 v[0:3], v[104:107], v[130:133], v[0:3]
	s_cbranch_scc0 .Lat0_O_1254
	v_mov_b32_e32 v189, v215
	v_mov_b32_e32 v198, v248
	s_nop 1
	v_permlane16_swap_b32_e32 v215, v189
	v_permlane16_swap_b32_e32 v248, v198
	v_add_f32_e32 v189, v215, v189
	v_add_f32_e32 v198, v248, v198
	v_mov_b32_e32 v217, v189
	v_mov_b32_e32 v250, v198
	s_nop 1
	v_permlane32_swap_b32_e32 v189, v217
	v_permlane32_swap_b32_e32 v198, v250
	v_add_f32_e32 v103, v189, v217
	v_add_f32_e32 v102, v198, v250
	s_branch .LBB0_1251

.Lat0_O_1256:
	s_andn2_b64 vcc, exec, s[18:19]
	s_cbranch_vccnz .Lat0_O_1258
	s_mov_b32 s34, s21
	s_mov_b32 m0, s34
	s_nop 0
	global_load_lds_dwordx4 v32, s[100:101]
	s_add_i32 m0, s34, 0x8000
	s_nop 0
	global_load_lds_dwordx4 v184, s[100:101]
	s_add_i32 m0, s34, 0x400
	s_nop 0
	global_load_lds_dwordx4 v186, s[100:101]
	s_add_i32 m0, s34, 0x8400
	s_nop 0
	global_load_lds_dwordx4 v188, s[100:101]
	s_add_u32 s100, s100, 0x240000
	s_addc_u32 s101, s101, 0
.Lat0_O_1258:
	ds_read_b128 v[102:105], v222 offset:16384
	ds_read_b128 v[106:109], v223 offset:16384
	ds_read_b128 v[110:113], v224 offset:16384
	ds_read_b128 v[114:117], v225 offset:16384
	ds_read_b128 v[118:121], v222 offset:20480
	ds_read_b128 v[122:125], v223 offset:20480
	ds_read_b128 v[126:129], v224 offset:20480
	ds_read_b128 v[130:133], v225 offset:20480
	s_waitcnt lgkmcnt(0)
	v_mfma_f32_16x16x32_bf16 v[138:141], v[118:121], v[78:81], 0
	v_mfma_f32_16x16x32_bf16 v[134:137], v[102:105], v[78:81], 0
	v_mfma_f32_16x16x32_bf16 v[102:105], v[102:105], v[94:97], 0
	v_mfma_f32_16x16x32_bf16 v[118:121], v[118:121], v[94:97], 0
	v_mfma_f32_16x16x32_bf16 v[134:137], v[106:109], v[70:73], v[134:137]
	v_mfma_f32_16x16x32_bf16 v[102:105], v[106:109], v[86:89], v[102:105]
	v_mfma_f32_16x16x32_bf16 v[138:141], v[122:125], v[70:73], v[138:141]
	v_mfma_f32_16x16x32_bf16 v[118:121], v[122:125], v[86:89], v[118:121]
	v_mfma_f32_16x16x32_bf16 v[134:137], v[110:113], v[74:77], v[134:137]
	v_mfma_f32_16x16x32_bf16 v[102:105], v[110:113], v[90:93], v[102:105]
	v_mfma_f32_16x16x32_bf16 v[138:141], v[126:129], v[74:77], v[138:141]
	v_mfma_f32_16x16x32_bf16 v[118:121], v[126:129], v[90:93], v[118:121]
	v_mfma_f32_16x16x32_bf16 v[162:165], v[114:117], v[82:85], v[134:137]
	v_mfma_f32_16x16x32_bf16 v[134:137], v[114:117], v[98:101], v[102:105]
	s_nop 3
	ds_read_b128 v[102:105], v222 offset:24576
	ds_read_b128 v[106:109], v223 offset:24576
	ds_read_b128 v[110:113], v224 offset:24576
	ds_read_b128 v[114:117], v225 offset:24576
	v_max_f32_e32 v187, v164, v165
	v_mfma_f32_16x16x32_bf16 v[158:161], v[130:133], v[82:85], v[138:141]
	v_max3_f32 v187, v162, v163, v187
	v_mfma_f32_16x16x32_bf16 v[138:141], v[130:133], v[98:101], v[118:121]
	s_nop 2
	ds_read_b128 v[118:121], v222 offset:28672
	ds_read_b128 v[122:125], v223 offset:28672
	ds_read_b128 v[126:129], v224 offset:28672
	ds_read_b128 v[130:133], v225 offset:28672
	v_max3_f32 v189, v159, v160, v161
	v_max3_f32 v187, v187, v158, v189
	s_waitcnt lgkmcnt(0)
	v_mfma_f32_16x16x32_bf16 v[142:145], v[102:105], v[78:81], 0
	v_mfma_f32_16x16x32_bf16 v[102:105], v[102:105], v[94:97], 0
	v_mfma_f32_16x16x32_bf16 v[102:105], v[106:109], v[86:89], v[102:105]
	v_mfma_f32_16x16x32_bf16 v[102:105], v[110:113], v[90:93], v[102:105]
	v_mfma_f32_16x16x32_bf16 v[146:149], v[114:117], v[98:101], v[102:105]
	v_mfma_f32_16x16x32_bf16 v[102:105], v[118:121], v[78:81], 0
	v_mfma_f32_16x16x32_bf16 v[142:145], v[106:109], v[70:73], v[142:145]
	v_mfma_f32_16x16x32_bf16 v[102:105], v[122:125], v[70:73], v[102:105]
	v_mfma_f32_16x16x32_bf16 v[142:145], v[110:113], v[74:77], v[142:145]
	v_mfma_f32_16x16x32_bf16 v[102:105], v[126:129], v[74:77], v[102:105]
	v_mfma_f32_16x16x32_bf16 v[154:157], v[114:117], v[82:85], v[142:145]
	v_mfma_f32_16x16x32_bf16 v[150:153], v[130:133], v[82:85], v[102:105]
	v_mfma_f32_16x16x32_bf16 v[102:105], v[118:121], v[94:97], 0
	s_nop 5
	v_max3_f32 v189, v155, v156, v157
	v_max3_f32 v187, v187, v154, v189
	v_max3_f32 v189, v151, v152, v153
	v_mfma_f32_16x16x32_bf16 v[102:105], v[122:125], v[86:89], v[102:105]
	v_max3_f32 v187, v187, v150, v189
	v_mov_b32_e32 v189, v187
	s_nop 1
	v_permlane16_swap_b32_e32 v187, v189
	v_mfma_f32_16x16x32_bf16 v[102:105], v[126:129], v[90:93], v[102:105]
	v_max_f32 v187, v187, v189
	s_nop 0
	v_mov_b32_e32 v189, v187
	s_nop 1
	v_permlane32_swap_b32_e32 v187, v189
	v_max_f32 v187, v187, v189
	v_mfma_f32_16x16x32_bf16 v[142:145], v[130:133], v[98:101], v[102:105]
	v_mul_f32_e32 v187, 0x3e0293ee, v187
	v_add_f32_e32 v189, 0x41000000, v218
	v_cmp_gt_f32_e32 vcc, v187, v189
	ds_read_b64_tr_b16 v[130:131], v237 offset:49152
	ds_read_b64_tr_b16 v[132:133], v237 offset:53248
	ds_read_b64_tr_b16 v[122:123], v237 offset:57344
	ds_read_b64_tr_b16 v[124:125], v237 offset:61440
	ds_read_b64_tr_b16 v[126:127], v238 offset:49152
	ds_read_b64_tr_b16 v[128:129], v238 offset:53248
	ds_read_b64_tr_b16 v[114:115], v238 offset:57344
	ds_read_b64_tr_b16 v[116:117], v238 offset:61440
	v_cndmask_b32_e32 v187, v218, v187, vcc
	ds_read_b64_tr_b16 v[118:119], v239 offset:49152
	ds_read_b64_tr_b16 v[120:121], v239 offset:53248
	ds_read_b64_tr_b16 v[110:111], v239 offset:57344
	ds_read_b64_tr_b16 v[112:113], v239 offset:61440
	ds_read_b64_tr_b16 v[106:107], v240 offset:49152
	ds_read_b64_tr_b16 v[108:109], v240 offset:53248
	ds_read_b64_tr_b16 v[102:103], v240 offset:57344
	ds_read_b64_tr_b16 v[104:105], v240 offset:61440
	ds_read_b64 v[198:199], v213
	v_fma_f32 v162, v162, s97, -v187
	v_exp_f32_e32 v162, v162
	v_fma_f32 v163, v163, s97, -v187
	v_exp_f32_e32 v163, v163
	v_fma_f32 v164, v164, s97, -v187
	v_exp_f32_e32 v164, v164
	v_fma_f32 v165, v165, s97, -v187
	v_exp_f32_e32 v165, v165
	v_fma_f32 v158, v158, s97, -v187
	s_waitcnt lgkmcnt(0)
	v_lshrrev_b64 v[216:217], v170, v[198:199]
	v_bfe_i32 v198, v216, 0, 1
	v_exp_f32_e32 v158, v158
	v_and_b32_e32 v162, v198, v162
	v_fma_f32 v159, v159, s97, -v187
	v_bfe_i32 v199, v216, 1, 1
	v_and_b32_e32 v163, v199, v163
	v_exp_f32_e32 v159, v159
	v_fma_f32 v160, v160, s97, -v187
	v_add_f32_e32 v198, v162, v163
	v_bfe_i32 v199, v216, 2, 1
	v_exp_f32_e32 v160, v160
	v_and_b32_e32 v164, v199, v164
	v_fma_f32 v161, v161, s97, -v187
	v_bfe_i32 v200, v216, 3, 1
	v_add_f32_e32 v198, v198, v164
	v_and_b32_e32 v165, v200, v165
	v_exp_f32_e32 v161, v161
	v_fma_f32 v154, v154, s97, -v187
	v_add_f32_e32 v198, v198, v165
	v_bfe_i32 v199, v216, 16, 1
	v_exp_f32_e32 v154, v154
	v_and_b32_e32 v158, v199, v158
	v_fma_f32 v155, v155, s97, -v187
	v_bfe_i32 v200, v216, 17, 1
	v_add_f32_e32 v198, v198, v158
	v_and_b32_e32 v159, v200, v159
	v_exp_f32_e32 v155, v155
	v_fma_f32 v156, v156, s97, -v187
	v_add_f32_e32 v198, v198, v159
	v_bfe_i32 v199, v216, 18, 1
	v_exp_f32_e32 v156, v156
	v_and_b32_e32 v160, v199, v160
	v_fma_f32 v157, v157, s97, -v187
	v_bfe_i32 v200, v216, 19, 1
	v_add_f32_e32 v198, v198, v160
	v_and_b32_e32 v161, v200, v161
	v_exp_f32_e32 v157, v157
	v_add_f32_e32 v198, v198, v161
	v_bfe_i32 v199, v217, 0, 1
	v_fma_f32 v150, v150, s97, -v187
	v_and_b32_e32 v154, v199, v154
	v_bfe_i32 v200, v217, 1, 1
	v_add_f32_e32 v198, v198, v154
	v_and_b32_e32 v155, v200, v155
	v_exp_f32_e32 v150, v150
	v_fma_f32 v151, v151, s97, -v187
	v_add_f32_e32 v198, v198, v155
	v_bfe_i32 v199, v217, 2, 1
	v_exp_f32_e32 v151, v151
	v_and_b32_e32 v216, v199, v156
	v_fma_f32 v152, v152, s97, -v187
	v_bfe_i32 v200, v217, 3, 1
	v_add_f32_e32 v156, v198, v216
	v_and_b32_e32 v157, v200, v157
	v_exp_f32_e32 v152, v152
	v_fma_f32 v153, v153, s97, -v187
	v_add_f32_e32 v198, v156, v157
	v_bfe_i32 v156, v217, 16, 1
	v_exp_f32_e32 v153, v153
	v_and_b32_e32 v156, v156, v150
	v_bfe_i32 v199, v217, 17, 1
	v_add_f32_e32 v150, v198, v156
	v_and_b32_e32 v151, v199, v151
	v_add_f32_e32 v150, v150, v151
	v_bfe_i32 v198, v217, 18, 1
	v_sub_f32_e32 v189, v218, v187
	v_and_b32_e32 v152, v198, v152
	v_bfe_i32 v199, v217, 19, 1
	v_add_f32_e32 v150, v150, v152
	v_and_b32_e32 v153, v199, v153
	v_add_f32_e32 v198, v150, v153
	v_exp_f32_e32 v150, v189
	s_nop 0
	v_cmp_eq_f32_e32 vcc, 1.0, v150
	v_fma_f32 v215, v215, v150, v198
	s_cmp_eq_u64 vcc, exec
	s_cbranch_scc1 .Lat0_O_1260
	v_pk_mul_f32 v[68:69], v[68:69], v[150:151] op_sel_hi:[1,0]
	v_pk_mul_f32 v[66:67], v[66:67], v[150:151] op_sel_hi:[1,0]
	v_pk_mul_f32 v[64:65], v[64:65], v[150:151] op_sel_hi:[1,0]
	v_pk_mul_f32 v[62:63], v[62:63], v[150:151] op_sel_hi:[1,0]
	v_pk_mul_f32 v[60:61], v[60:61], v[150:151] op_sel_hi:[1,0]
	v_pk_mul_f32 v[58:59], v[58:59], v[150:151] op_sel_hi:[1,0]
	v_pk_mul_f32 v[56:57], v[56:57], v[150:151] op_sel_hi:[1,0]
	v_pk_mul_f32 v[54:55], v[54:55], v[150:151] op_sel_hi:[1,0]
	v_pk_mul_f32 v[52:53], v[52:53], v[150:151] op_sel_hi:[1,0]
	v_pk_mul_f32 v[50:51], v[50:51], v[150:151] op_sel_hi:[1,0]
	v_pk_mul_f32 v[48:49], v[48:49], v[150:151] op_sel_hi:[1,0]
	v_pk_mul_f32 v[46:47], v[46:47], v[150:151] op_sel_hi:[1,0]
	v_pk_mul_f32 v[44:45], v[44:45], v[150:151] op_sel_hi:[1,0]
	v_pk_mul_f32 v[42:43], v[42:43], v[150:151] op_sel_hi:[1,0]
	v_pk_mul_f32 v[40:41], v[40:41], v[150:151] op_sel_hi:[1,0]
	v_pk_mul_f32 v[38:39], v[38:39], v[150:151] op_sel_hi:[1,0]

.Lat0_O_1262:
	v_cvt_pk_bf16_f32 v162, v162, v163
	v_cvt_pk_bf16_f32 v163, v164, v165
	v_cvt_pk_bf16_f32 v164, v158, v159
	v_cvt_pk_bf16_f32 v165, v160, v161
	v_cvt_pk_bf16_f32 v158, v218, v167
	v_cvt_pk_bf16_f32 v159, v136, v135
	v_cvt_pk_bf16_f32 v160, v138, v137
	v_cvt_pk_bf16_f32 v161, v140, v139
	v_mfma_f32_16x16x32_bf16 v[54:57], v[106:109], v[162:165], v[54:57]
	v_cvt_pk_bf16_f32 v154, v154, v155
	v_cvt_pk_bf16_f32 v155, v216, v157
	v_cvt_pk_bf16_f32 v156, v156, v151
	v_mfma_f32_16x16x32_bf16 v[16:19], v[106:109], v[158:161], v[16:19]
	v_cvt_pk_bf16_f32 v157, v152, v153
	s_add_i32 s31, s31, 1
	v_mfma_f32_16x16x32_bf16 v[66:69], v[130:133], v[162:165], v[66:69]
	v_add_u32_e32 v213, 8, v213
	s_cmp_eq_u32 s30, s31
	v_mfma_f32_16x16x32_bf16 v[28:31], v[130:133], v[158:161], v[28:31]
	v_cvt_pk_bf16_f32 v130, v146, v141
	v_cvt_pk_bf16_f32 v131, v148, v147
	v_cvt_pk_bf16_f32 v132, v142, v143
	v_cvt_pk_bf16_f32 v133, v144, v145
	v_mfma_f32_16x16x32_bf16 v[54:57], v[102:105], v[154:157], v[54:57]
	s_nop 0
	v_mfma_f32_16x16x32_bf16 v[16:19], v[102:105], v[130:133], v[16:19]
	ds_read_b64_tr_b16 v[102:103], v241 offset:49152
	ds_read_b64_tr_b16 v[104:105], v241 offset:53248
	ds_read_b64_tr_b16 v[106:107], v241 offset:57344
	ds_read_b64_tr_b16 v[108:109], v241 offset:61440
	v_mfma_f32_16x16x32_bf16 v[58:61], v[118:121], v[162:165], v[58:61]
	v_mfma_f32_16x16x32_bf16 v[20:23], v[118:121], v[158:161], v[20:23]
	s_waitcnt lgkmcnt(2)
	v_mfma_f32_16x16x32_bf16 v[50:53], v[102:105], v[162:165], v[50:53]
	v_mfma_f32_16x16x32_bf16 v[12:15], v[102:105], v[158:161], v[12:15]
	v_mfma_f32_16x16x32_bf16 v[58:61], v[110:113], v[154:157], v[58:61]
	v_mfma_f32_16x16x32_bf16 v[20:23], v[110:113], v[130:133], v[20:23]
	s_waitcnt lgkmcnt(0)
	v_mfma_f32_16x16x32_bf16 v[50:53], v[106:109], v[154:157], v[50:53]
	v_mfma_f32_16x16x32_bf16 v[12:15], v[106:109], v[130:133], v[12:15]
	ds_read_b64_tr_b16 v[102:103], v242 offset:49152
	ds_read_b64_tr_b16 v[104:105], v242 offset:53248
	ds_read_b64_tr_b16 v[106:107], v242 offset:57344
	ds_read_b64_tr_b16 v[108:109], v242 offset:61440
	s_waitcnt lgkmcnt(2)
	v_mfma_f32_16x16x32_bf16 v[46:49], v[102:105], v[162:165], v[46:49]
	v_mfma_f32_16x16x32_bf16 v[8:11], v[102:105], v[158:161], v[8:11]
	s_waitcnt lgkmcnt(0)
	v_mfma_f32_16x16x32_bf16 v[46:49], v[106:109], v[154:157], v[46:49]
	v_mfma_f32_16x16x32_bf16 v[8:11], v[106:109], v[130:133], v[8:11]
	ds_read_b64_tr_b16 v[102:103], v243 offset:49152
	ds_read_b64_tr_b16 v[104:105], v243 offset:53248
	ds_read_b64_tr_b16 v[106:107], v243 offset:57344
	ds_read_b64_tr_b16 v[108:109], v243 offset:61440
	s_waitcnt lgkmcnt(2)
	v_mfma_f32_16x16x32_bf16 v[42:45], v[102:105], v[162:165], v[42:45]
	v_mfma_f32_16x16x32_bf16 v[4:7], v[102:105], v[158:161], v[4:7]
	ds_read_b64_tr_b16 v[110:111], v244 offset:49152
	ds_read_b64_tr_b16 v[112:113], v244 offset:53248
	s_waitcnt lgkmcnt(2)
	v_mfma_f32_16x16x32_bf16 v[42:45], v[106:109], v[154:157], v[42:45]
	v_mfma_f32_16x16x32_bf16 v[4:7], v[106:109], v[130:133], v[4:7]
	ds_read_b64_tr_b16 v[104:105], v244 offset:57344
	ds_read_b64_tr_b16 v[106:107], v244 offset:61440
	s_waitcnt vmcnt(0)
	v_mfma_f32_16x16x32_bf16 v[62:65], v[126:129], v[162:165], v[62:65]
	s_waitcnt lgkmcnt(0)
	s_barrier
	v_mfma_f32_16x16x32_bf16 v[24:27], v[126:129], v[158:161], v[24:27]
	v_mfma_f32_16x16x32_bf16 v[38:41], v[110:113], v[162:165], v[38:41]
	v_mfma_f32_16x16x32_bf16 v[0:3], v[110:113], v[158:161], v[0:3]
	v_mfma_f32_16x16x32_bf16 v[66:69], v[122:125], v[154:157], v[66:69]
	v_mfma_f32_16x16x32_bf16 v[28:31], v[122:125], v[130:133], v[28:31]
	v_mfma_f32_16x16x32_bf16 v[62:65], v[114:117], v[154:157], v[62:65]
	v_mfma_f32_16x16x32_bf16 v[24:27], v[114:117], v[130:133], v[24:27]
	v_mfma_f32_16x16x32_bf16 v[38:41], v[104:107], v[154:157], v[38:41]
	v_mfma_f32_16x16x32_bf16 v[0:3], v[104:107], v[130:133], v[0:3]
	s_cbranch_scc0 .LBB0_1254
	v_mov_b32_e32 v189, v215
	v_mov_b32_e32 v198, v248
	s_nop 1
	v_permlane16_swap_b32_e32 v215, v189
	v_permlane16_swap_b32_e32 v248, v198
	v_add_f32_e32 v189, v215, v189
	v_add_f32_e32 v198, v248, v198
	v_mov_b32_e32 v217, v189
	v_mov_b32_e32 v250, v198
	s_nop 1
	v_permlane32_swap_b32_e32 v189, v217
	v_permlane32_swap_b32_e32 v198, v250
	v_add_f32_e32 v103, v189, v217
	v_add_f32_e32 v102, v198, v250
	s_branch .LBB0_1251
